# LN kernels rewritten by hand (all loads issued up front, same arithmetic order) on top of wconv128 + cache-policy stores + 4-phase GEMM loops
# speedup vs baseline: 1.0328x; 1.0050x over previous
_Z9ln_kernelILb0ELb0EEvPKvPKtS3_PKfPvPtS5_S5_:
	s_load_dwordx8 s[4:11], s[0:1], 0x0
	s_load_dwordx8 s[12:19], s[0:1], 0x20
	v_lshlrev_b32_e32 v1, 3, v0
	v_lshlrev_b32_e32 v2, 4, v0
	v_or_b32_e32 v3, 0x1000, v2
	s_lshl_b32 s20, s2, 12
	s_lshl_b32 s21, s2, 13
	s_waitcnt lgkmcnt(0)
	s_cmp_lg_u64 s[6:7], 0
	s_cselect_b32 s22, 1, 0
	s_cmp_lg_u64 s[10:11], 0
	s_cselect_b32 s23, 1, 0
	s_cmp_lg_u64 s[12:13], 0
	s_cselect_b32 s24, 1, 0
	s_cmp_lg_u64 s[14:15], 0
	s_cselect_b32 s25, 1, 0
	s_add_u32 s4, s4, s21
	s_addc_u32 s5, s5, 0
	s_add_u32 s6, s6, s20
	s_addc_u32 s7, s7, 0
	s_add_u32 s8, s8, s20
	s_addc_u32 s9, s9, 0
	s_add_u32 s12, s12, s21
	s_addc_u32 s13, s13, 0
	s_add_u32 s14, s14, s20
	s_addc_u32 s15, s15, 0
	s_cmp_eq_u32 s22, 0
	s_cbranch_scc1 .Lln00_nop0
	global_load_dwordx2 v[12:13], v1, s[6:7] nt
	global_load_dwordx2 v[14:15], v1, s[6:7] offset:2048 nt
	global_load_dwordx2 v[16:17], v1, s[8:9] nt
	global_load_dwordx2 v[18:19], v1, s[8:9] offset:2048 nt
.Lln00_nop0:
	s_cmp_eq_u32 s23, 0
	s_cbranch_scc1 .Lln00_nob0
	global_load_dwordx4 v[20:23], v2, s[10:11]
	global_load_dwordx4 v[24:27], v3, s[10:11]
.Lln00_nob0:
	global_load_dwordx4 v[44:47], v2, s[4:5] nt
	global_load_dwordx4 v[48:51], v3, s[4:5] nt
	s_cmp_eq_u32 s25, 0
	s_cbranch_scc1 .Lln00_noln0
	global_load_dwordx4 v[28:31], v2, s[16:17]
	global_load_dwordx4 v[32:35], v3, s[16:17]
	global_load_dwordx4 v[36:39], v2, s[18:19]
	global_load_dwordx4 v[40:43], v3, s[18:19]
	v_and_b32_e32 v60, 63, v0
	v_xor_b32_e32 v52, 32, v60
	v_xor_b32_e32 v53, 16, v60
	v_xor_b32_e32 v54, 8, v60
	v_xor_b32_e32 v55, 4, v60
	v_xor_b32_e32 v56, 2, v60
	v_xor_b32_e32 v57, 1, v60
	v_lshlrev_b32_e32 v52, 2, v52
	v_lshlrev_b32_e32 v53, 2, v53
	v_lshlrev_b32_e32 v54, 2, v54
	v_lshlrev_b32_e32 v55, 2, v55
	v_lshlrev_b32_e32 v56, 2, v56
	v_lshlrev_b32_e32 v57, 2, v57
	v_lshrrev_b32_e32 v61, 4, v0
	s_waitcnt vmcnt(4)
	s_branch .Lln00_go

.Lln00_go:
	s_cmp_eq_u32 s22, 0
	s_cbranch_scc1 .Lln00_nop1
	v_cvt_f32_f16_e32 v4, v12
	v_cvt_f32_f16_sdwa v5, v12 dst_sel:DWORD dst_unused:UNUSED_PAD src0_sel:WORD_1
	v_cvt_f32_f16_e32 v6, v13
	v_cvt_f32_f16_sdwa v7, v13 dst_sel:DWORD dst_unused:UNUSED_PAD src0_sel:WORD_1
	v_cvt_f32_f16_e32 v8, v16
	v_cvt_f32_f16_sdwa v9, v16 dst_sel:DWORD dst_unused:UNUSED_PAD src0_sel:WORD_1
	v_cvt_f32_f16_e32 v10, v17
	v_cvt_f32_f16_sdwa v11, v17 dst_sel:DWORD dst_unused:UNUSED_PAD src0_sel:WORD_1
	s_nop 0
	v_pk_add_f32 v[4:5], v[4:5], v[8:9]
	v_pk_add_f32 v[6:7], v[6:7], v[10:11]
	s_nop 0
	v_pk_add_f32 v[44:45], v[4:5], v[44:45]
	v_pk_add_f32 v[46:47], v[6:7], v[46:47]
	v_cvt_f32_f16_e32 v4, v14
	v_cvt_f32_f16_sdwa v5, v14 dst_sel:DWORD dst_unused:UNUSED_PAD src0_sel:WORD_1
	v_cvt_f32_f16_e32 v6, v15
	v_cvt_f32_f16_sdwa v7, v15 dst_sel:DWORD dst_unused:UNUSED_PAD src0_sel:WORD_1
	v_cvt_f32_f16_e32 v8, v18
	v_cvt_f32_f16_sdwa v9, v18 dst_sel:DWORD dst_unused:UNUSED_PAD src0_sel:WORD_1
	v_cvt_f32_f16_e32 v10, v19
	v_cvt_f32_f16_sdwa v11, v19 dst_sel:DWORD dst_unused:UNUSED_PAD src0_sel:WORD_1
	s_nop 0
	v_pk_add_f32 v[4:5], v[4:5], v[8:9]
	v_pk_add_f32 v[6:7], v[6:7], v[10:11]
	s_nop 0
	v_pk_add_f32 v[48:49], v[4:5], v[48:49]
	v_pk_add_f32 v[50:51], v[6:7], v[50:51]
.Lln00_nop1:
	s_cmp_eq_u32 s23, 0
	s_cbranch_scc1 .Lln00_nob1
	s_nop 0
	v_pk_add_f32 v[44:45], v[44:45], v[20:21]
	v_pk_add_f32 v[46:47], v[46:47], v[22:23]
	v_pk_add_f32 v[48:49], v[48:49], v[24:25]
	v_pk_add_f32 v[50:51], v[50:51], v[26:27]
.Lln00_nob1:
	s_cmp_eq_u32 s24, 0
	s_cbranch_scc1 .Lln00_noys
	s_nop 0
	global_store_dwordx4 v2, v[44:47], s[12:13] sc1
	global_store_dwordx4 v3, v[48:51], s[12:13] sc1
.Lln00_noys:
	s_cmp_eq_u32 s25, 0
	s_cbranch_scc1 .Lln00_end
	v_add_f32_e32 v4, v44, v45
	v_add_f32_e32 v5, v48, v49
	v_add_f32_e32 v4, v46, v4
	v_add_f32_e32 v5, v50, v5
	v_add_f32_e32 v4, v47, v4
	v_add_f32_e32 v5, v51, v5
	v_add_f32_e32 v4, 0, v4
	v_add_f32_e32 v4, v4, v5
	ds_bpermute_b32 v5, v52, v4
	s_waitcnt lgkmcnt(0)
	v_add_f32_e32 v4, v4, v5
	ds_bpermute_b32 v5, v53, v4
	s_waitcnt lgkmcnt(0)
	v_add_f32_e32 v4, v4, v5
	ds_bpermute_b32 v5, v54, v4
	s_waitcnt lgkmcnt(0)
	v_add_f32_e32 v4, v4, v5
	ds_bpermute_b32 v5, v55, v4
	s_waitcnt lgkmcnt(0)
	v_add_f32_e32 v4, v4, v5
	ds_bpermute_b32 v5, v56, v4
	s_waitcnt lgkmcnt(0)
	v_add_f32_e32 v4, v4, v5
	ds_bpermute_b32 v5, v57, v4
	s_waitcnt lgkmcnt(0)
	v_add_f32_e32 v4, v4, v5
	v_cmp_eq_u32_e32 vcc, 0, v60
	s_and_saveexec_b64 s[26:27], vcc
	ds_write_b32 v61, v4
	s_or_b64 exec, exec, s[26:27]
	v_mov_b32_e32 v9, 0
	s_waitcnt lgkmcnt(0)
	s_barrier
	ds_read_b128 v[4:7], v9
	s_waitcnt lgkmcnt(0)
	s_barrier
	v_add_f32_e32 v8, v4, v5
	v_add_f32_e32 v8, v8, v6
	v_add_f32_e32 v8, v8, v7
	v_mul_f32_e32 v10, 0x3a000000, v8
	s_nop 0
	v_pk_add_f32 v[44:45], v[44:45], v[10:11] op_sel_hi:[1,0] neg_lo:[0,1] neg_hi:[0,1]
	v_pk_add_f32 v[46:47], v[46:47], v[10:11] op_sel_hi:[1,0] neg_lo:[0,1] neg_hi:[0,1]
	v_pk_add_f32 v[48:49], v[48:49], v[10:11] op_sel_hi:[1,0] neg_lo:[0,1] neg_hi:[0,1]
	v_pk_add_f32 v[50:51], v[50:51], v[10:11] op_sel_hi:[1,0] neg_lo:[0,1] neg_hi:[0,1]
	s_nop 0
	v_pk_mul_f32 v[12:13], v[44:45], v[44:45]
	v_pk_mul_f32 v[14:15], v[46:47], v[46:47]
	v_pk_mul_f32 v[16:17], v[48:49], v[48:49]
	v_pk_mul_f32 v[18:19], v[50:51], v[50:51]
	v_add_f32_e32 v4, v12, v13
	v_add_f32_e32 v4, v4, v14
	v_add_f32_e32 v4, v4, v15
	v_add_f32_e32 v4, v4, v16
	v_add_f32_e32 v4, v4, v17
	v_add_f32_e32 v4, v4, v18
	v_add_f32_e32 v4, v4, v19
	ds_bpermute_b32 v5, v52, v4
	s_waitcnt lgkmcnt(0)
	v_add_f32_e32 v4, v4, v5
	ds_bpermute_b32 v5, v53, v4
	s_waitcnt lgkmcnt(0)
	v_add_f32_e32 v4, v4, v5
	ds_bpermute_b32 v5, v54, v4
	s_waitcnt lgkmcnt(0)
	v_add_f32_e32 v4, v4, v5
	ds_bpermute_b32 v5, v55, v4
	s_waitcnt lgkmcnt(0)
	v_add_f32_e32 v4, v4, v5
	ds_bpermute_b32 v5, v56, v4
	s_waitcnt lgkmcnt(0)
	v_add_f32_e32 v4, v4, v5
	ds_bpermute_b32 v5, v57, v4
	s_waitcnt lgkmcnt(0)
	v_add_f32_e32 v4, v4, v5
	v_cmp_eq_u32_e32 vcc, 0, v60
	s_and_saveexec_b64 s[26:27], vcc
	ds_write_b32 v61, v4
	s_or_b64 exec, exec, s[26:27]
	v_mov_b32_e32 v9, 0
	s_waitcnt lgkmcnt(0)
	s_barrier
	ds_read_b128 v[4:7], v9
	s_waitcnt lgkmcnt(0)
	v_add_f32_e32 v8, v4, v5
	v_add_f32_e32 v8, v8, v6
	v_add_f32_e32 v8, v8, v7
	v_mov_b32_e32 v10, 0x3727c5ac
	v_fmac_f32_e32 v10, 0x3a000000, v8
	s_mov_b32 s26, 0x800000
	v_mul_f32_e32 v12, 0x4b800000, v10
	v_cmp_gt_f32_e32 vcc, s26, v10
	s_nop 1
	v_cndmask_b32_e32 v12, v10, v12, vcc
	v_rsq_f32_e32 v12, v12
	s_nop 0
	v_mul_f32_e32 v14, 0x45800000, v12
	v_cndmask_b32_e32 v12, v12, v14, vcc
	s_nop 0
	v_pk_mul_f32 v[44:45], v[12:13], v[44:45] op_sel_hi:[0,1]
	v_pk_mul_f32 v[46:47], v[12:13], v[46:47] op_sel_hi:[0,1]
	v_pk_mul_f32 v[48:49], v[12:13], v[48:49] op_sel_hi:[0,1]
	v_pk_mul_f32 v[50:51], v[12:13], v[50:51] op_sel_hi:[0,1]
	s_waitcnt vmcnt(0)
	v_pk_fma_f32 v[44:45], v[28:29], v[44:45], v[36:37]
	v_pk_fma_f32 v[46:47], v[30:31], v[46:47], v[38:39]
	v_pk_fma_f32 v[48:49], v[32:33], v[48:49], v[40:41]
	v_pk_fma_f32 v[50:51], v[34:35], v[50:51], v[42:43]
	v_cvt_pk_f16_f32 v4, v44, v45
	v_cvt_pk_f16_f32 v5, v46, v47
	v_cvt_pk_f16_f32 v6, v48, v49
	v_cvt_pk_f16_f32 v7, v50, v51
	global_store_dwordx2 v1, v[4:5], s[14:15] sc1
	global_store_dwordx2 v1, v[6:7], s[14:15] offset:2048 sc1

	.amdhsa_kernel _Z9ln_kernelILb0ELb0EEvPKvPKtS3_PKfPvPtS5_S5_
		.amdhsa_group_segment_fixed_size 16
		.amdhsa_private_segment_fixed_size 0
		.amdhsa_kernarg_size 64
		.amdhsa_user_sgpr_count 2
		.amdhsa_user_sgpr_dispatch_ptr 0
		.amdhsa_user_sgpr_queue_ptr 0
		.amdhsa_user_sgpr_kernarg_segment_ptr 1
		.amdhsa_user_sgpr_dispatch_id 0
		.amdhsa_user_sgpr_kernarg_preload_length 0
		.amdhsa_user_sgpr_kernarg_preload_offset 0
		.amdhsa_user_sgpr_private_segment_size 0
		.amdhsa_uses_dynamic_stack 0
		.amdhsa_enable_private_segment 0
		.amdhsa_system_sgpr_workgroup_id_x 1
		.amdhsa_system_sgpr_workgroup_id_y 0
		.amdhsa_system_sgpr_workgroup_id_z 0
		.amdhsa_system_sgpr_workgroup_info 0
		.amdhsa_system_vgpr_workitem_id 0
		.amdhsa_next_free_vgpr 62
		.amdhsa_next_free_sgpr 28
		.amdhsa_accum_offset 64
		.amdhsa_reserve_vcc 1
		.amdhsa_float_round_mode_32 0
		.amdhsa_float_round_mode_16_64 0
		.amdhsa_float_denorm_mode_32 3
		.amdhsa_float_denorm_mode_16_64 3
		.amdhsa_dx10_clamp 1
		.amdhsa_ieee_mode 1
		.amdhsa_fp16_overflow 0
		.amdhsa_tg_split 0
		.amdhsa_exception_fp_ieee_invalid_op 0
		.amdhsa_exception_fp_denorm_src 0
		.amdhsa_exception_fp_ieee_div_zero 0
		.amdhsa_exception_fp_ieee_overflow 0
		.amdhsa_exception_fp_ieee_underflow 0
		.amdhsa_exception_fp_ieee_inexact 0
		.amdhsa_exception_int_div_zero 0
	.end_amdhsa_kernel

_Z9ln_kernelILb1ELb1EEvPKvPKtS3_PKfPvPtS5_S5_:
	s_load_dwordx8 s[4:11], s[0:1], 0x0
	s_load_dwordx8 s[12:19], s[0:1], 0x20
	v_lshlrev_b32_e32 v1, 3, v0
	v_lshlrev_b32_e32 v2, 4, v0
	v_or_b32_e32 v3, 0x1000, v2
	s_lshl_b32 s20, s2, 12
	s_lshl_b32 s21, s2, 13
	s_waitcnt lgkmcnt(0)
	s_cmp_lg_u64 s[6:7], 0
	s_cselect_b32 s22, 1, 0
	s_cmp_lg_u64 s[10:11], 0
	s_cselect_b32 s23, 1, 0
	s_cmp_lg_u64 s[12:13], 0
	s_cselect_b32 s24, 1, 0
	s_cmp_lg_u64 s[14:15], 0
	s_cselect_b32 s25, 1, 0
	s_add_u32 s4, s4, s20
	s_addc_u32 s5, s5, 0
	s_add_u32 s6, s6, s20
	s_addc_u32 s7, s7, 0
	s_add_u32 s8, s8, s20
	s_addc_u32 s9, s9, 0
	s_add_u32 s12, s12, s20
	s_addc_u32 s13, s13, 0
	s_add_u32 s14, s14, s20
	s_addc_u32 s15, s15, 0
	s_cmp_eq_u32 s22, 0
	s_cbranch_scc1 .Lln11_nop0
	global_load_dwordx2 v[12:13], v1, s[6:7] nt
	global_load_dwordx2 v[14:15], v1, s[6:7] offset:2048 nt
	global_load_dwordx2 v[16:17], v1, s[8:9] nt
	global_load_dwordx2 v[18:19], v1, s[8:9] offset:2048 nt

.Lln11_nob0:
	global_load_dwordx2 v[4:5], v1, s[4:5] nt
	global_load_dwordx2 v[6:7], v1, s[4:5] offset:2048 nt
	s_cmp_eq_u32 s25, 0
	s_cbranch_scc1 .Lln11_noln0
	global_load_dwordx4 v[28:31], v2, s[16:17]
	global_load_dwordx4 v[32:35], v3, s[16:17]
	global_load_dwordx4 v[36:39], v2, s[18:19]
	global_load_dwordx4 v[40:43], v3, s[18:19]
	v_and_b32_e32 v60, 63, v0
	v_xor_b32_e32 v52, 32, v60
	v_xor_b32_e32 v53, 16, v60
	v_xor_b32_e32 v54, 8, v60
	v_xor_b32_e32 v55, 4, v60
	v_xor_b32_e32 v56, 2, v60
	v_xor_b32_e32 v57, 1, v60
	v_lshlrev_b32_e32 v52, 2, v52
	v_lshlrev_b32_e32 v53, 2, v53
	v_lshlrev_b32_e32 v54, 2, v54
	v_lshlrev_b32_e32 v55, 2, v55
	v_lshlrev_b32_e32 v56, 2, v56
	v_lshlrev_b32_e32 v57, 2, v57
	v_lshrrev_b32_e32 v61, 4, v0
	s_waitcnt vmcnt(4)
	s_branch .Lln11_go

.Lln11_go:
	v_cvt_f32_f16_e32 v44, v4
	v_cvt_f32_f16_sdwa v45, v4 dst_sel:DWORD dst_unused:UNUSED_PAD src0_sel:WORD_1
	v_cvt_f32_f16_e32 v46, v5
	v_cvt_f32_f16_sdwa v47, v5 dst_sel:DWORD dst_unused:UNUSED_PAD src0_sel:WORD_1
	v_cvt_f32_f16_e32 v48, v6
	v_cvt_f32_f16_sdwa v49, v6 dst_sel:DWORD dst_unused:UNUSED_PAD src0_sel:WORD_1
	v_cvt_f32_f16_e32 v50, v7
	v_cvt_f32_f16_sdwa v51, v7 dst_sel:DWORD dst_unused:UNUSED_PAD src0_sel:WORD_1
	s_cmp_eq_u32 s22, 0
	s_cbranch_scc1 .Lln11_nop1
	v_cvt_f32_f16_e32 v4, v12
	v_cvt_f32_f16_sdwa v5, v12 dst_sel:DWORD dst_unused:UNUSED_PAD src0_sel:WORD_1
	v_cvt_f32_f16_e32 v6, v13
	v_cvt_f32_f16_sdwa v7, v13 dst_sel:DWORD dst_unused:UNUSED_PAD src0_sel:WORD_1
	v_cvt_f32_f16_e32 v8, v16
	v_cvt_f32_f16_sdwa v9, v16 dst_sel:DWORD dst_unused:UNUSED_PAD src0_sel:WORD_1
	v_cvt_f32_f16_e32 v10, v17
	v_cvt_f32_f16_sdwa v11, v17 dst_sel:DWORD dst_unused:UNUSED_PAD src0_sel:WORD_1
	s_nop 0
	v_pk_add_f32 v[4:5], v[4:5], v[8:9]
	v_pk_add_f32 v[6:7], v[6:7], v[10:11]
	s_nop 0
	v_pk_add_f32 v[44:45], v[4:5], v[44:45]
	v_pk_add_f32 v[46:47], v[6:7], v[46:47]
	v_cvt_f32_f16_e32 v4, v14
	v_cvt_f32_f16_sdwa v5, v14 dst_sel:DWORD dst_unused:UNUSED_PAD src0_sel:WORD_1
	v_cvt_f32_f16_e32 v6, v15
	v_cvt_f32_f16_sdwa v7, v15 dst_sel:DWORD dst_unused:UNUSED_PAD src0_sel:WORD_1
	v_cvt_f32_f16_e32 v8, v18
	v_cvt_f32_f16_sdwa v9, v18 dst_sel:DWORD dst_unused:UNUSED_PAD src0_sel:WORD_1
	v_cvt_f32_f16_e32 v10, v19
	v_cvt_f32_f16_sdwa v11, v19 dst_sel:DWORD dst_unused:UNUSED_PAD src0_sel:WORD_1
	s_nop 0
	v_pk_add_f32 v[4:5], v[4:5], v[8:9]
	v_pk_add_f32 v[6:7], v[6:7], v[10:11]
	s_nop 0
	v_pk_add_f32 v[48:49], v[4:5], v[48:49]
	v_pk_add_f32 v[50:51], v[6:7], v[50:51]

.Lln11_nob1:
	s_cmp_eq_u32 s24, 0
	s_cbranch_scc1 .Lln11_noys
	s_nop 0
	v_cvt_pk_f16_f32 v4, v44, v45
	v_cvt_pk_f16_f32 v5, v46, v47
	v_cvt_pk_f16_f32 v6, v48, v49
	v_cvt_pk_f16_f32 v7, v50, v51
	global_store_dwordx2 v1, v[4:5], s[12:13] sc1
	global_store_dwordx2 v1, v[6:7], s[12:13] offset:2048 sc1
	v_cvt_f32_f16_e32 v44, v4
	v_cvt_f32_f16_sdwa v45, v4 dst_sel:DWORD dst_unused:UNUSED_PAD src0_sel:WORD_1
	v_cvt_f32_f16_e32 v46, v5
	v_cvt_f32_f16_sdwa v47, v5 dst_sel:DWORD dst_unused:UNUSED_PAD src0_sel:WORD_1
	v_cvt_f32_f16_e32 v48, v6
	v_cvt_f32_f16_sdwa v49, v6 dst_sel:DWORD dst_unused:UNUSED_PAD src0_sel:WORD_1
	v_cvt_f32_f16_e32 v50, v7
	v_cvt_f32_f16_sdwa v51, v7 dst_sel:DWORD dst_unused:UNUSED_PAD src0_sel:WORD_1

	.amdhsa_kernel _Z9ln_kernelILb1ELb1EEvPKvPKtS3_PKfPvPtS5_S5_
		.amdhsa_group_segment_fixed_size 16
		.amdhsa_private_segment_fixed_size 0
		.amdhsa_kernarg_size 64
		.amdhsa_user_sgpr_count 2
		.amdhsa_user_sgpr_dispatch_ptr 0
		.amdhsa_user_sgpr_queue_ptr 0
		.amdhsa_user_sgpr_kernarg_segment_ptr 1
		.amdhsa_user_sgpr_dispatch_id 0
		.amdhsa_user_sgpr_kernarg_preload_length 0
		.amdhsa_user_sgpr_kernarg_preload_offset 0
		.amdhsa_user_sgpr_private_segment_size 0
		.amdhsa_uses_dynamic_stack 0
		.amdhsa_enable_private_segment 0
		.amdhsa_system_sgpr_workgroup_id_x 1
		.amdhsa_system_sgpr_workgroup_id_y 0
		.amdhsa_system_sgpr_workgroup_id_z 0
		.amdhsa_system_sgpr_workgroup_info 0
		.amdhsa_system_vgpr_workitem_id 0
		.amdhsa_next_free_vgpr 62
		.amdhsa_next_free_sgpr 28
		.amdhsa_accum_offset 64
		.amdhsa_reserve_vcc 1
		.amdhsa_float_round_mode_32 0
		.amdhsa_float_round_mode_16_64 0
		.amdhsa_float_denorm_mode_32 3
		.amdhsa_float_denorm_mode_16_64 3
		.amdhsa_dx10_clamp 1
		.amdhsa_ieee_mode 1
		.amdhsa_fp16_overflow 0
		.amdhsa_tg_split 0
		.amdhsa_exception_fp_ieee_invalid_op 0
		.amdhsa_exception_fp_denorm_src 0
		.amdhsa_exception_fp_ieee_div_zero 0
		.amdhsa_exception_fp_ieee_overflow 0
		.amdhsa_exception_fp_ieee_underflow 0
		.amdhsa_exception_fp_ieee_inexact 0
		.amdhsa_exception_int_div_zero 0
	.end_amdhsa_kernel

_Z9ln_kernelILb0ELb1EEvPKvPKtS3_PKfPvPtS5_S5_:
	s_load_dwordx8 s[4:11], s[0:1], 0x0
	s_load_dwordx8 s[12:19], s[0:1], 0x20
	v_lshlrev_b32_e32 v1, 3, v0
	v_lshlrev_b32_e32 v2, 4, v0
	v_or_b32_e32 v3, 0x1000, v2
	s_lshl_b32 s20, s2, 12
	s_lshl_b32 s21, s2, 13
	s_waitcnt lgkmcnt(0)
	s_cmp_lg_u64 s[6:7], 0
	s_cselect_b32 s22, 1, 0
	s_cmp_lg_u64 s[10:11], 0
	s_cselect_b32 s23, 1, 0
	s_cmp_lg_u64 s[12:13], 0
	s_cselect_b32 s24, 1, 0
	s_cmp_lg_u64 s[14:15], 0
	s_cselect_b32 s25, 1, 0
	s_add_u32 s4, s4, s21
	s_addc_u32 s5, s5, 0
	s_add_u32 s6, s6, s20
	s_addc_u32 s7, s7, 0
	s_add_u32 s8, s8, s20
	s_addc_u32 s9, s9, 0
	s_add_u32 s12, s12, s20
	s_addc_u32 s13, s13, 0
	s_add_u32 s14, s14, s20
	s_addc_u32 s15, s15, 0
	s_cmp_eq_u32 s22, 0
	s_cbranch_scc1 .Lln01_nop0
	global_load_dwordx2 v[12:13], v1, s[6:7] nt
	global_load_dwordx2 v[14:15], v1, s[6:7] offset:2048 nt
	global_load_dwordx2 v[16:17], v1, s[8:9] nt
	global_load_dwordx2 v[18:19], v1, s[8:9] offset:2048 nt

	.amdhsa_kernel _Z9ln_kernelILb0ELb1EEvPKvPKtS3_PKfPvPtS5_S5_
		.amdhsa_group_segment_fixed_size 16
		.amdhsa_private_segment_fixed_size 0
		.amdhsa_kernarg_size 64
		.amdhsa_user_sgpr_count 2
		.amdhsa_user_sgpr_dispatch_ptr 0
		.amdhsa_user_sgpr_queue_ptr 0
		.amdhsa_user_sgpr_kernarg_segment_ptr 1
		.amdhsa_user_sgpr_dispatch_id 0
		.amdhsa_user_sgpr_kernarg_preload_length 0
		.amdhsa_user_sgpr_kernarg_preload_offset 0
		.amdhsa_user_sgpr_private_segment_size 0
		.amdhsa_uses_dynamic_stack 0
		.amdhsa_enable_private_segment 0
		.amdhsa_system_sgpr_workgroup_id_x 1
		.amdhsa_system_sgpr_workgroup_id_y 0
		.amdhsa_system_sgpr_workgroup_id_z 0
		.amdhsa_system_sgpr_workgroup_info 0
		.amdhsa_system_vgpr_workitem_id 0
		.amdhsa_next_free_vgpr 62
		.amdhsa_next_free_sgpr 28
		.amdhsa_accum_offset 64
		.amdhsa_reserve_vcc 1
		.amdhsa_float_round_mode_32 0
		.amdhsa_float_round_mode_16_64 0
		.amdhsa_float_denorm_mode_32 3
		.amdhsa_float_denorm_mode_16_64 3
		.amdhsa_dx10_clamp 1
		.amdhsa_ieee_mode 1
		.amdhsa_fp16_overflow 0
		.amdhsa_tg_split 0
		.amdhsa_exception_fp_ieee_invalid_op 0
		.amdhsa_exception_fp_denorm_src 0
		.amdhsa_exception_fp_ieee_div_zero 0
		.amdhsa_exception_fp_ieee_overflow 0
		.amdhsa_exception_fp_ieee_underflow 0
		.amdhsa_exception_fp_ieee_inexact 0
		.amdhsa_exception_int_div_zero 0
	.end_amdhsa_kernel

_Z9ln_kernelILb1ELb0EEvPKvPKtS3_PKfPvPtS5_S5_:
	s_load_dwordx8 s[4:11], s[0:1], 0x0
	s_load_dwordx8 s[12:19], s[0:1], 0x20
	v_lshlrev_b32_e32 v1, 3, v0
	v_lshlrev_b32_e32 v2, 4, v0
	v_or_b32_e32 v3, 0x1000, v2
	s_lshl_b32 s20, s2, 12
	s_lshl_b32 s21, s2, 13
	s_waitcnt lgkmcnt(0)
	s_cmp_lg_u64 s[6:7], 0
	s_cselect_b32 s22, 1, 0
	s_cmp_lg_u64 s[10:11], 0
	s_cselect_b32 s23, 1, 0
	s_cmp_lg_u64 s[12:13], 0
	s_cselect_b32 s24, 1, 0
	s_cmp_lg_u64 s[14:15], 0
	s_cselect_b32 s25, 1, 0
	s_add_u32 s4, s4, s20
	s_addc_u32 s5, s5, 0
	s_add_u32 s6, s6, s20
	s_addc_u32 s7, s7, 0
	s_add_u32 s8, s8, s20
	s_addc_u32 s9, s9, 0
	s_add_u32 s12, s12, s21
	s_addc_u32 s13, s13, 0
	s_add_u32 s14, s14, s20
	s_addc_u32 s15, s15, 0
	s_cmp_eq_u32 s22, 0
	s_cbranch_scc1 .Lln10_nop0
	global_load_dwordx2 v[12:13], v1, s[6:7] nt
	global_load_dwordx2 v[14:15], v1, s[6:7] offset:2048 nt
	global_load_dwordx2 v[16:17], v1, s[8:9] nt
	global_load_dwordx2 v[18:19], v1, s[8:9] offset:2048 nt

	.amdhsa_kernel _Z9ln_kernelILb1ELb0EEvPKvPKtS3_PKfPvPtS5_S5_
		.amdhsa_group_segment_fixed_size 16
		.amdhsa_private_segment_fixed_size 0
		.amdhsa_kernarg_size 64
		.amdhsa_user_sgpr_count 2
		.amdhsa_user_sgpr_dispatch_ptr 0
		.amdhsa_user_sgpr_queue_ptr 0
		.amdhsa_user_sgpr_kernarg_segment_ptr 1
		.amdhsa_user_sgpr_dispatch_id 0
		.amdhsa_user_sgpr_kernarg_preload_length 0
		.amdhsa_user_sgpr_kernarg_preload_offset 0
		.amdhsa_user_sgpr_private_segment_size 0
		.amdhsa_uses_dynamic_stack 0
		.amdhsa_enable_private_segment 0
		.amdhsa_system_sgpr_workgroup_id_x 1
		.amdhsa_system_sgpr_workgroup_id_y 0
		.amdhsa_system_sgpr_workgroup_id_z 0
		.amdhsa_system_sgpr_workgroup_info 0
		.amdhsa_system_vgpr_workitem_id 0
		.amdhsa_next_free_vgpr 62
		.amdhsa_next_free_sgpr 28
		.amdhsa_accum_offset 64
		.amdhsa_reserve_vcc 1
		.amdhsa_float_round_mode_32 0
		.amdhsa_float_round_mode_16_64 0
		.amdhsa_float_denorm_mode_32 3
		.amdhsa_float_denorm_mode_16_64 3
		.amdhsa_dx10_clamp 1
		.amdhsa_ieee_mode 1
		.amdhsa_fp16_overflow 0
		.amdhsa_tg_split 0
		.amdhsa_exception_fp_ieee_invalid_op 0
		.amdhsa_exception_fp_denorm_src 0
		.amdhsa_exception_fp_ieee_div_zero 0
		.amdhsa_exception_fp_ieee_overflow 0
		.amdhsa_exception_fp_ieee_underflow 0
		.amdhsa_exception_fp_ieee_inexact 0
		.amdhsa_exception_int_div_zero 0
	.end_amdhsa_kernel

amdhsa.kernels:
  - .agpr_count:     0
    .args:
      - .offset:         0
        .size:           336
        .value_kind:     by_value
      - .offset:         336
        .size:           4
        .value_kind:     by_value
    .group_segment_fixed_size: 32768
    .kernarg_segment_align: 8
    .kernarg_segment_size: 340
    .language:       OpenCL C
    .language_version:
      - 2
      - 0
    .max_flat_workgroup_size: 256
    .name:           _Z12wconv_kernel5WDesci
    .private_segment_fixed_size: 0
    .sgpr_count:     36
    .sgpr_spill_count: 0
    .symbol:         _Z12wconv_kernel5WDesci.kd
    .uniform_work_group_size: 1
    .uses_dynamic_stack: false
    .vgpr_count:     103
    .vgpr_spill_count: 0
    .wavefront_size: 64
  - .agpr_count:     160
    .args:
      - .actual_access:  read_only
        .address_space:  global
        .offset:         0
        .size:           8
        .value_kind:     global_buffer
      - .address_space:  global
        .offset:         8
        .size:           8
        .value_kind:     global_buffer
      - .address_space:  global
        .offset:         16
        .size:           8
        .value_kind:     global_buffer
      - .actual_access:  read_only
        .address_space:  global
        .offset:         24
        .size:           8
        .value_kind:     global_buffer
      - .actual_access:  read_only
        .address_space:  global
        .offset:         32
        .size:           8
        .value_kind:     global_buffer
      - .actual_access:  read_only
        .address_space:  global
        .offset:         40
        .size:           8
        .value_kind:     global_buffer
      - .actual_access:  write_only
        .address_space:  global
        .offset:         48
        .size:           8
        .value_kind:     global_buffer
    .group_segment_fixed_size: 0
    .kernarg_segment_align: 8
    .kernarg_segment_size: 56
    .language:       OpenCL C
    .language_version:
      - 2
      - 0
    .max_flat_workgroup_size: 256
    .name:           _Z8ret_fastPKtS0_S0_S0_PKfS2_Pt
    .private_segment_fixed_size: 0
    .sgpr_count:     85
    .sgpr_spill_count: 0
    .symbol:         _Z8ret_fastPKtS0_S0_S0_PKfS2_Pt.kd
    .uniform_work_group_size: 1
    .uses_dynamic_stack: false
    .vgpr_count:     348
    .vgpr_spill_count: 0
    .wavefront_size: 64
  - .agpr_count:     0
    .args:
      - .actual_access:  read_only
        .address_space:  global
        .offset:         0
        .size:           8
        .value_kind:     global_buffer
      - .actual_access:  read_only
        .address_space:  global
        .offset:         8
        .size:           8
        .value_kind:     global_buffer
      - .actual_access:  read_only
        .address_space:  global
        .offset:         16
        .size:           8
        .value_kind:     global_buffer
      - .actual_access:  read_only
        .address_space:  global
        .offset:         24
        .size:           8
        .value_kind:     global_buffer
      - .actual_access:  write_only
        .address_space:  global
        .offset:         32
        .size:           8
        .value_kind:     global_buffer
      - .actual_access:  write_only
        .address_space:  global
        .offset:         40
        .size:           8
        .value_kind:     global_buffer
      - .actual_access:  read_only
        .address_space:  global
        .offset:         48
        .size:           8
        .value_kind:     global_buffer
      - .actual_access:  read_only
        .address_space:  global
        .offset:         56
        .size:           8
        .value_kind:     global_buffer
    .group_segment_fixed_size: 16
    .kernarg_segment_align: 8
    .kernarg_segment_size: 64
    .language:       OpenCL C
    .language_version:
      - 2
      - 0
    .max_flat_workgroup_size: 256
    .name:           _Z9ln_kernelILb0ELb0EEvPKvPKtS3_PKfPvPtS5_S5_
    .private_segment_fixed_size: 0
    .sgpr_count:     34
    .sgpr_spill_count: 0
    .symbol:         _Z9ln_kernelILb0ELb0EEvPKvPKtS3_PKfPvPtS5_S5_.kd
    .uniform_work_group_size: 1
    .uses_dynamic_stack: false
    .vgpr_count:     62
    .vgpr_spill_count: 0
    .wavefront_size: 64
  - .agpr_count:     0
    .args:
      - .actual_access:  read_only
        .address_space:  global
        .offset:         0
        .size:           8
        .value_kind:     global_buffer
      - .actual_access:  read_only
        .address_space:  global
        .offset:         8
        .size:           8
        .value_kind:     global_buffer
      - .actual_access:  read_only
        .address_space:  global
        .offset:         16
        .size:           8
        .value_kind:     global_buffer
      - .actual_access:  read_only
        .address_space:  global
        .offset:         24
        .size:           8
        .value_kind:     global_buffer
      - .actual_access:  write_only
        .address_space:  global
        .offset:         32
        .size:           8
        .value_kind:     global_buffer
      - .actual_access:  write_only
        .address_space:  global
        .offset:         40
        .size:           8
        .value_kind:     global_buffer
      - .actual_access:  read_only
        .address_space:  global
        .offset:         48
        .size:           8
        .value_kind:     global_buffer
      - .actual_access:  read_only
        .address_space:  global
        .offset:         56
        .size:           8
        .value_kind:     global_buffer
    .group_segment_fixed_size: 16
    .kernarg_segment_align: 8
    .kernarg_segment_size: 64
    .language:       OpenCL C
    .language_version:
      - 2
      - 0
    .max_flat_workgroup_size: 256
    .name:           _Z9ln_kernelILb1ELb1EEvPKvPKtS3_PKfPvPtS5_S5_
    .private_segment_fixed_size: 0
    .sgpr_count:     34
    .sgpr_spill_count: 0
    .symbol:         _Z9ln_kernelILb1ELb1EEvPKvPKtS3_PKfPvPtS5_S5_.kd
    .uniform_work_group_size: 1
    .uses_dynamic_stack: false
    .vgpr_count:     62
    .vgpr_spill_count: 0
    .wavefront_size: 64
  - .agpr_count:     0
    .args:
      - .address_space:  global
        .offset:         0
        .size:           8
        .value_kind:     global_buffer
      - .address_space:  global
        .offset:         8
        .size:           8
        .value_kind:     global_buffer
      - .offset:         16
        .size:           4
        .value_kind:     by_value
      - .offset:         20
        .size:           4
        .value_kind:     by_value
      - .offset:         24
        .size:           4
        .value_kind:     by_value
      - .offset:         28
        .size:           4
        .value_kind:     by_value
      - .offset:         32
        .size:           40
        .value_kind:     by_value
      - .offset:         72
        .size:           4
        .value_kind:     hidden_block_count_x
      - .offset:         76
        .size:           4
        .value_kind:     hidden_block_count_y
      - .offset:         80
        .size:           4
        .value_kind:     hidden_block_count_z
      - .offset:         84
        .size:           2
        .value_kind:     hidden_group_size_x
      - .offset:         86
        .size:           2
        .value_kind:     hidden_group_size_y
      - .offset:         88
        .size:           2
        .value_kind:     hidden_group_size_z
      - .offset:         90
        .size:           2
        .value_kind:     hidden_remainder_x
      - .offset:         92
        .size:           2
        .value_kind:     hidden_remainder_y
      - .offset:         94
        .size:           2
        .value_kind:     hidden_remainder_z
      - .offset:         112
        .size:           8
        .value_kind:     hidden_global_offset_x
      - .offset:         120
        .size:           8
        .value_kind:     hidden_global_offset_y
      - .offset:         128
        .size:           8
        .value_kind:     hidden_global_offset_z
      - .offset:         136
        .size:           2
        .value_kind:     hidden_grid_dims
      - .offset:         192
        .size:           4
        .value_kind:     hidden_dynamic_lds_size
    .group_segment_fixed_size: 0
    .kernarg_segment_align: 8
    .kernarg_segment_size: 328
    .language:       OpenCL C
    .language_version:
      - 2
      - 0
    .max_flat_workgroup_size: 512
    .name:           _Z9gemm_fastILi0ELi2EEvPKtS1_iiii7EpiArgs
    .private_segment_fixed_size: 0
    .sgpr_count:     55
    .sgpr_spill_count: 0
    .symbol:         _Z9gemm_fastILi0ELi2EEvPKtS1_iiii7EpiArgs.kd
    .uniform_work_group_size: 1
    .uses_dynamic_stack: false
    .vgpr_count:     255
    .vgpr_spill_count: 0
    .wavefront_size: 64
  - .agpr_count:     0
    .args:
      - .address_space:  global
        .offset:         0
        .size:           8
        .value_kind:     global_buffer
      - .address_space:  global
        .offset:         8
        .size:           8
        .value_kind:     global_buffer
      - .offset:         16
        .size:           4
        .value_kind:     by_value
      - .offset:         20
        .size:           4
        .value_kind:     by_value
      - .offset:         24
        .size:           4
        .value_kind:     by_value
      - .offset:         28
        .size:           4
        .value_kind:     by_value
      - .offset:         32
        .size:           40
        .value_kind:     by_value
    .group_segment_fixed_size: 0
    .kernarg_segment_align: 8
    .kernarg_segment_size: 72
    .language:       OpenCL C
    .language_version:
      - 2
      - 0
    .max_flat_workgroup_size: 512
    .name:           _Z9gemm_fastILi1ELi1EEvPKtS1_iiii7EpiArgs
    .private_segment_fixed_size: 0
    .sgpr_count:     32
    .sgpr_spill_count: 0
    .symbol:         _Z9gemm_fastILi1ELi1EEvPKtS1_iiii7EpiArgs.kd
    .uniform_work_group_size: 1
    .uses_dynamic_stack: false
    .vgpr_count:     247
    .vgpr_spill_count: 0
    .wavefront_size: 64
  - .agpr_count:     0
    .args:
      - .actual_access:  read_only
        .address_space:  global
        .offset:         0
        .size:           8
        .value_kind:     global_buffer
      - .actual_access:  read_only
        .address_space:  global
        .offset:         8
        .size:           8
        .value_kind:     global_buffer
      - .actual_access:  read_only
        .address_space:  global
        .offset:         16
        .size:           8
        .value_kind:     global_buffer
      - .actual_access:  read_only
        .address_space:  global
        .offset:         24
        .size:           8
        .value_kind:     global_buffer
      - .actual_access:  write_only
        .address_space:  global
        .offset:         32
        .size:           8
        .value_kind:     global_buffer
      - .actual_access:  write_only
        .address_space:  global
        .offset:         40
        .size:           8
        .value_kind:     global_buffer
      - .actual_access:  read_only
        .address_space:  global
        .offset:         48
        .size:           8
        .value_kind:     global_buffer
      - .actual_access:  read_only
        .address_space:  global
        .offset:         56
        .size:           8
        .value_kind:     global_buffer
    .group_segment_fixed_size: 16
    .kernarg_segment_align: 8
    .kernarg_segment_size: 64
    .language:       OpenCL C
    .language_version:
      - 2
      - 0
    .max_flat_workgroup_size: 256
    .name:           _Z9ln_kernelILb0ELb1EEvPKvPKtS3_PKfPvPtS5_S5_
    .private_segment_fixed_size: 0
    .sgpr_count:     34
    .sgpr_spill_count: 0
    .symbol:         _Z9ln_kernelILb0ELb1EEvPKvPKtS3_PKfPvPtS5_S5_.kd
    .uniform_work_group_size: 1
    .uses_dynamic_stack: false
    .vgpr_count:     62
    .vgpr_spill_count: 0
    .wavefront_size: 64
  - .agpr_count:     0
    .args:
      - .address_space:  global
        .offset:         0
        .size:           8
        .value_kind:     global_buffer
      - .address_space:  global
        .offset:         8
        .size:           8
        .value_kind:     global_buffer
      - .offset:         16
        .size:           4
        .value_kind:     by_value
      - .offset:         20
        .size:           4
        .value_kind:     by_value
      - .offset:         24
        .size:           4
        .value_kind:     by_value
      - .offset:         28
        .size:           4
        .value_kind:     by_value
      - .offset:         32
        .size:           40
        .value_kind:     by_value
      - .offset:         72
        .size:           4
        .value_kind:     hidden_block_count_x
      - .offset:         76
        .size:           4
        .value_kind:     hidden_block_count_y
      - .offset:         80
        .size:           4
        .value_kind:     hidden_block_count_z
      - .offset:         84
        .size:           2
        .value_kind:     hidden_group_size_x
      - .offset:         86
        .size:           2
        .value_kind:     hidden_group_size_y
      - .offset:         88
        .size:           2
        .value_kind:     hidden_group_size_z
      - .offset:         90
        .size:           2
        .value_kind:     hidden_remainder_x
      - .offset:         92
        .size:           2
        .value_kind:     hidden_remainder_y
      - .offset:         94
        .size:           2
        .value_kind:     hidden_remainder_z
      - .offset:         112
        .size:           8
        .value_kind:     hidden_global_offset_x
      - .offset:         120
        .size:           8
        .value_kind:     hidden_global_offset_y
      - .offset:         128
        .size:           8
        .value_kind:     hidden_global_offset_z
      - .offset:         136
        .size:           2
        .value_kind:     hidden_grid_dims
      - .offset:         192
        .size:           4
        .value_kind:     hidden_dynamic_lds_size
    .group_segment_fixed_size: 0
    .kernarg_segment_align: 8
    .kernarg_segment_size: 328
    .language:       OpenCL C
    .language_version:
      - 2
      - 0
    .max_flat_workgroup_size: 512
    .name:           _Z9gemm_fastILi2ELi2EEvPKtS1_iiii7EpiArgs
    .private_segment_fixed_size: 0
    .sgpr_count:     53
    .sgpr_spill_count: 0
    .symbol:         _Z9gemm_fastILi2ELi2EEvPKtS1_iiii7EpiArgs.kd
    .uniform_work_group_size: 1
    .uses_dynamic_stack: false
    .vgpr_count:     248
    .vgpr_spill_count: 0
    .wavefront_size: 64
  - .agpr_count:     0
    .args:
      - .actual_access:  read_only
        .address_space:  global
        .offset:         0
        .size:           8
        .value_kind:     global_buffer
      - .actual_access:  read_only
        .address_space:  global
        .offset:         8
        .size:           8
        .value_kind:     global_buffer
      - .actual_access:  read_only
        .address_space:  global
        .offset:         16
        .size:           8
        .value_kind:     global_buffer
      - .actual_access:  read_only
        .address_space:  global
        .offset:         24
        .size:           8
        .value_kind:     global_buffer
      - .actual_access:  write_only
        .address_space:  global
        .offset:         32
        .size:           8
        .value_kind:     global_buffer
      - .actual_access:  write_only
        .address_space:  global
        .offset:         40
        .size:           8
        .value_kind:     global_buffer
      - .actual_access:  read_only
        .address_space:  global
        .offset:         48
        .size:           8
        .value_kind:     global_buffer
      - .actual_access:  read_only
        .address_space:  global
        .offset:         56
        .size:           8
        .value_kind:     global_buffer
    .group_segment_fixed_size: 16
    .kernarg_segment_align: 8
    .kernarg_segment_size: 64
    .language:       OpenCL C
    .language_version:
      - 2
      - 0
    .max_flat_workgroup_size: 256
    .name:           _Z9ln_kernelILb1ELb0EEvPKvPKtS3_PKfPvPtS5_S5_
    .private_segment_fixed_size: 0
    .sgpr_count:     34
    .sgpr_spill_count: 0
    .symbol:         _Z9ln_kernelILb1ELb0EEvPKvPKtS3_PKfPvPtS5_S5_.kd
    .uniform_work_group_size: 1
    .uses_dynamic_stack: false
    .vgpr_count:     62
    .vgpr_spill_count: 0
    .wavefront_size: 64
